# baseline (speedup 1.0000x reference)
_Z12giou_partialPK15HIP_vector_typeIfLj4EES2_S2_PKiPS_IfLj2EE:
	s_load_dwordx8 s[16:23], s[0:1], 0x0
	s_load_dwordx2 s[24:25], s[0:1], 0x20
	s_cmpk_ge_u32 s2, 0x100
	s_cbranch_scc1 .Llate_block
	s_movk_i32 s3, 0x200
	s_lshl_b32 s6, s2, 10
	v_cmp_gt_u32_e32 vcc, s3, v0
	v_lshlrev_b32_e32 v11, 4, v0
	v_lshrrev_b32_e32 v1, 6, v0
	v_and_b32_e32 v10, 63, v0
	v_lshl_add_u32 v6, v1, 18, s6
	v_lshlrev_b32_e32 v8, 2, v6
	v_lshl_add_u32 v8, v10, 4, v8
	s_lshl_b32 s7, s2, 14
	v_readfirstlane_b32 s15, v1
	v_add_u32_e32 v43, 0x200, v6
	s_waitcnt lgkmcnt(0)
	s_add_u32 s20, s20, s7
	s_addc_u32 s21, s21, 0
	global_load_dwordx4 v[12:15], v8, s[22:23] nt
	global_load_dwordx4 v[16:19], v8, s[22:23] offset:1024 nt
	global_load_dwordx4 v[26:29], v8, s[22:23] offset:2048 nt
	global_load_dwordx4 v[30:33], v8, s[22:23] offset:3072 nt
	s_and_saveexec_b64 s[8:9], vcc
	s_cbranch_execz .Lno_anc
	v_add_u32_e32 v9, 0x2000, v11
	global_load_dwordx4 v[2:5], v11, s[20:21] nt
	global_load_dwordx4 v[44:47], v9, s[20:21] nt
.Lno_anc:
	s_or_b64 exec, exec, s[8:9]
	v_mov_b32_e32 v7, 0x80
	s_waitcnt vmcnt(0)
	s_sub_u32 s26, 0xff, s2
	s_mul_i32 s26, s26, 15
	s_lshr_b32 s26, s26, 7
	s_min_u32 s26, s26, 64
	s_cmp_eq_u32 s26, 0
	s_cbranch_scc1 .Lhold_done

.LcompA_end:
	s_or_b64 exec, exec, s[10:11]
	s_ashr_i32 s0, s14, 16
	s_add_i32 s3, s3, s0
	s_mov_b32 s27, s3
	v_mov_b32_e32 v12, v26
	v_mov_b32_e32 v13, v27
	v_mov_b32_e32 v14, v28
	v_mov_b32_e32 v15, v29
	v_mov_b32_e32 v16, v30
	v_mov_b32_e32 v17, v31
	v_mov_b32_e32 v18, v32
	v_mov_b32_e32 v19, v33
	v_mov_b32_e32 v7, 0x80
	v_cmp_ne_u32_e64 s[4:5], 0, v12
	s_nop 1
	v_cndmask_b32_e64 v8, 0, 1, s[4:5]
	v_cmp_eq_u32_e64 s[4:5], 0, v13
	s_nop 1
	v_cndmask_b32_e64 v9, 2, 0, s[4:5]
	v_cmp_eq_u32_e64 s[4:5], 0, v14
	v_or_b32_e32 v8, v9, v8
	s_nop 0
	v_cndmask_b32_e64 v12, 4, 0, s[4:5]
	v_cmp_eq_u32_e64 s[4:5], 0, v15
	s_nop 1
	v_cndmask_b32_e64 v13, 8, 0, s[4:5]
	v_cmp_eq_u32_e64 s[4:5], 0, v16
	v_or3_b32 v8, v8, v12, v13
	s_nop 0
	v_cndmask_b32_e64 v14, 16, 0, s[4:5]
	v_cmp_eq_u32_e64 s[4:5], 0, v17
	s_nop 1
	v_cndmask_b32_e64 v15, 32, 0, s[4:5]
	v_cmp_eq_u32_e64 s[4:5], 0, v18
	s_nop 1
	v_cndmask_b32_e64 v16, 64, 0, s[4:5]
	v_cmp_eq_u32_e64 s[4:5], 0, v19
	s_nop 1
	v_cndmask_b32_e64 v7, v7, 0, s[4:5]
	v_or_b32_e32 v7, v16, v7
	v_or3_b32 v9, v7, v15, v14
	v_or_b32_e32 v7, v9, v8
	v_bcnt_u32_b32 v8, v8, 0
	v_bcnt_u32_b32 v9, v9, 0
	v_lshl_or_b32 v9, v9, 16, v8
	v_cmp_ne_u32_e64 s[4:5], 0, v7
	s_nop 0
	v_add_u32_dpp v8, v9, v9 row_shr:1 row_mask:0xf bank_mask:0xf bound_ctrl:1
	s_nop 1
	v_add_u32_dpp v8, v8, v8 row_shr:2 row_mask:0xf bank_mask:0xf bound_ctrl:1
	s_nop 1
	v_add_u32_dpp v8, v8, v8 row_shr:4 row_mask:0xf bank_mask:0xf bound_ctrl:1
	s_nop 1
	v_add_u32_dpp v12, v8, v8 row_shr:8 row_mask:0xf bank_mask:0xf bound_ctrl:1
	s_nop 1
	v_add_u32_dpp v12, v12, v12 row_bcast:15 row_mask:0xa bank_mask:0xf
	s_nop 1
	v_add_u32_dpp v12, v12, v12 row_bcast:31 row_mask:0xc bank_mask:0xf
	s_nop 0
	v_readlane_b32 s14, v12, 63
	s_and_b32 s3, s14, 0xffff
	s_and_saveexec_b64 s[10:11], s[4:5]
	s_cbranch_execz .LcompB_end
	v_sub_u32_e32 v12, v12, v9
	v_lshlrev_b32_e32 v8, 10, v1
	v_add_u32_sdwa v9, sext(v12), s3 dst_sel:DWORD dst_unused:UNUSED_PAD src0_sel:WORD_1 src1_sel:DWORD
	v_and_b32_e32 v12, 0xffff, v12
	v_lshlrev_b32_e32 v13, 2, v10
	s_mov_b64 s[12:13], 0
	v_mov_b32_e32 v14, 0x100
.LcompB_loop:
	v_ffbl_b32_e32 v15, v7
	v_add_u32_e32 v16, -1, v7
	v_cmp_gt_u32_e64 s[4:5], 4, v15
	v_and_b32_e32 v18, 3, v15
	v_cmp_lt_u32_e64 s[6:7], 3, v15
	v_cndmask_b32_e64 v17, v9, v12, s[4:5]
	v_and_b32_e32 v7, v16, v7
	v_cndmask_b32_e64 v15, v14, 0, s[4:5]
	v_addc_co_u32_e64 v12, s[4:5], 0, v12, s[4:5]
	v_cmp_eq_u32_e64 s[4:5], 0, v7
	v_addc_co_u32_e64 v9, s[6:7], 0, v9, s[6:7]
	v_lshl_add_u32 v16, v17, 1, v8
	v_or3_b32 v15, v18, v13, v15
	s_or_b64 s[12:13], s[4:5], s[12:13]
	ds_write_b16 v16, v15 offset:16384
	s_andn2_b64 exec, exec, s[12:13]
	s_cbranch_execnz .LcompB_loop
.LcompB_end:
	s_or_b64 exec, exec, s[10:11]
	s_ashr_i32 s0, s14, 16
	s_add_i32 s3, s3, s0
	s_mov_b32 s28, s3
	s_and_saveexec_b64 s[0:1], vcc
	ds_write_b128 v11, v[2:5] offset:32768
	ds_write_b128 v11, v[44:47] offset:40960
	s_or_b64 exec, exec, s[0:1]
	s_waitcnt lgkmcnt(0)
	v_mov_b32_e32 v2, 0
	v_cmp_gt_i32_e32 vcc, s27, v10
	s_and_b64 exec, exec, vcc
	s_mov_b64 s[30:31], exec
	s_cbranch_execz .Lskip_issueA
	v_lshlrev_b32_e32 v3, 1, v10
	v_lshl_or_b32 v3, v1, 10, v3
	v_mov_b32_e32 v4, v10
	ds_read_u16 v5, v3
	s_waitcnt lgkmcnt(0)
	v_add_u32_e32 v8, v6, v5
	v_lshlrev_b32_e32 v8, 4, v8
	global_load_dwordx4 v[12:15], v8, s[16:17] nt
	global_load_dwordx4 v[16:19], v8, s[18:19] nt
	v_lshlrev_b32_e32 v5, 4, v5
.Lskip_issueA:
	s_mov_b64 exec, -1
	v_cmp_gt_i32_e32 vcc, s28, v10
	s_and_b64 exec, exec, vcc
	s_mov_b64 s[32:33], exec
	s_cbranch_execz .Lskip_issueB
	v_lshlrev_b32_e32 v24, 1, v10
	v_lshl_or_b32 v24, v1, 10, v24
	v_mov_b32_e32 v25, v10
	ds_read_u16 v42, v24 offset:16384
	s_waitcnt lgkmcnt(0)
	v_add_u32_e32 v8, v43, v42
	v_lshlrev_b32_e32 v8, 4, v8
	global_load_dwordx4 v[34:37], v8, s[16:17] nt
	global_load_dwordx4 v[38:41], v8, s[18:19] nt
	v_lshlrev_b32_e32 v42, 4, v42
.Lskip_issueB:
	s_mov_b64 exec, -1
	s_barrier
	s_waitcnt vmcnt(0)
	s_mov_b64 exec, s[30:31]
	s_cbranch_execz .Lskip_compA
	ds_read_b128 v[20:23], v5 offset:32768
	s_waitcnt lgkmcnt(0)
	v_pk_add_f32 v[8:9], v[22:23], v[20:21] neg_lo:[0,1] neg_hi:[0,1]
	s_nop 0
	v_pk_fma_f32 v[20:21], v[8:9], 0.5, v[20:21] op_sel_hi:[1,0,1]
	s_waitcnt vmcnt(1)
	v_mul_f32_e32 v5, 0x3fb8aa3b, v14
	v_mul_f32_e32 v7, 0x3fb8aa3b, v15
	v_pk_fma_f32 v[12:13], v[12:13], v[8:9], v[20:21]
	s_waitcnt vmcnt(0)
	v_sub_f32_e32 v14, v18, v16
	v_sub_f32_e32 v20, v19, v17
	v_max_f32_e32 v11, v18, v18
	v_max_f32_e32 v15, v16, v16
	v_max_f32_e32 v18, v19, v19
	v_max_f32_e32 v19, v17, v17
	v_exp_f32_e32 v16, v5
	v_exp_f32_e32 v17, v7
	s_nop 0
	v_pk_mul_f32 v[8:9], v[16:17], v[8:9]
	s_nop 0
	v_pk_fma_f32 v[16:17], v[8:9], 0.5, v[12:13] op_sel_hi:[1,0,1] neg_lo:[1,0,0] neg_hi:[1,0,0]
	v_pk_fma_f32 v[8:9], v[8:9], 0.5, v[12:13] op_sel_hi:[1,0,1]
	v_max_f32_e32 v7, v16, v15
	v_min_f32_e32 v5, v8, v11
	v_min_f32_e32 v21, v9, v18
	v_max_f32_e32 v22, v17, v19
	v_pk_add_f32 v[12:13], v[8:9], v[16:17] neg_lo:[0,1] neg_hi:[0,1]
	v_max_f32_e32 v8, v8, v11
	v_min_f32_e32 v11, v16, v15
	v_max_f32_e32 v9, v9, v18
	v_min_f32_e32 v15, v17, v19
	v_sub_f32_e32 v5, v5, v7
	v_sub_f32_e32 v7, v21, v22
	v_sub_f32_e32 v8, v8, v11
	v_sub_f32_e32 v9, v9, v15
	v_max_f32_e32 v15, 0, v5
	v_max_f32_e32 v21, 0, v7
	v_max_f32_e32 v5, 0, v8
	v_max_f32_e32 v7, 0, v9
	v_pk_mul_f32 v[8:9], v[14:15], v[20:21]
	v_mul_f32_e32 v11, v5, v7
	v_fma_f32 v8, v12, v13, v8
	v_sub_f32_e32 v8, v8, v9
	v_rcp_f32_e32 v14, v11
	v_rcp_f32_e32 v15, v8
	v_fma_f32 v8, v5, v7, -v8
	v_pk_mul_f32 v[8:9], v[14:15], v[8:9]
	s_nop 0
	v_sub_f32_e32 v5, v8, v9
	v_add_f32_e32 v5, 1.0, v5
	v_add_f32_e32 v2, v2, v5
.Lskip_compA:
	s_mov_b64 exec, s[32:33]
	s_cbranch_execz .Lskip_compB
	v_mov_b32_e32 v12, v34
	v_mov_b32_e32 v13, v35
	v_mov_b32_e32 v14, v36
	v_mov_b32_e32 v15, v37
	v_mov_b32_e32 v16, v38
	v_mov_b32_e32 v17, v39
	v_mov_b32_e32 v18, v40
	v_mov_b32_e32 v19, v41
	v_mov_b32_e32 v5, v42
	ds_read_b128 v[20:23], v5 offset:40960
	s_waitcnt lgkmcnt(0)
	v_pk_add_f32 v[8:9], v[22:23], v[20:21] neg_lo:[0,1] neg_hi:[0,1]
	s_nop 0
	v_pk_fma_f32 v[20:21], v[8:9], 0.5, v[20:21] op_sel_hi:[1,0,1]
	s_waitcnt vmcnt(1)
	v_mul_f32_e32 v5, 0x3fb8aa3b, v14
	v_mul_f32_e32 v7, 0x3fb8aa3b, v15
	v_pk_fma_f32 v[12:13], v[12:13], v[8:9], v[20:21]
	s_waitcnt vmcnt(0)
	v_sub_f32_e32 v14, v18, v16
	v_sub_f32_e32 v20, v19, v17
	v_max_f32_e32 v11, v18, v18
	v_max_f32_e32 v15, v16, v16
	v_max_f32_e32 v18, v19, v19
	v_max_f32_e32 v19, v17, v17
	v_exp_f32_e32 v16, v5
	v_exp_f32_e32 v17, v7
	s_nop 0
	v_pk_mul_f32 v[8:9], v[16:17], v[8:9]
	s_nop 0
	v_pk_fma_f32 v[16:17], v[8:9], 0.5, v[12:13] op_sel_hi:[1,0,1] neg_lo:[1,0,0] neg_hi:[1,0,0]
	v_pk_fma_f32 v[8:9], v[8:9], 0.5, v[12:13] op_sel_hi:[1,0,1]
	v_max_f32_e32 v7, v16, v15
	v_min_f32_e32 v5, v8, v11
	v_min_f32_e32 v21, v9, v18
	v_max_f32_e32 v22, v17, v19
	v_pk_add_f32 v[12:13], v[8:9], v[16:17] neg_lo:[0,1] neg_hi:[0,1]
	v_max_f32_e32 v8, v8, v11
	v_min_f32_e32 v11, v16, v15
	v_max_f32_e32 v9, v9, v18
	v_min_f32_e32 v15, v17, v19
	v_sub_f32_e32 v5, v5, v7
	v_sub_f32_e32 v7, v21, v22
	v_sub_f32_e32 v8, v8, v11
	v_sub_f32_e32 v9, v9, v15
	v_max_f32_e32 v15, 0, v5
	v_max_f32_e32 v21, 0, v7
	v_max_f32_e32 v5, 0, v8
	v_max_f32_e32 v7, 0, v9
	v_pk_mul_f32 v[8:9], v[14:15], v[20:21]
	v_mul_f32_e32 v11, v5, v7
	v_fma_f32 v8, v12, v13, v8
	v_sub_f32_e32 v8, v8, v9
	v_rcp_f32_e32 v14, v11
	v_rcp_f32_e32 v15, v8
	v_fma_f32 v8, v5, v7, -v8
	v_pk_mul_f32 v[8:9], v[14:15], v[8:9]
	s_nop 0
	v_sub_f32_e32 v5, v8, v9
	v_add_f32_e32 v5, 1.0, v5
	v_add_f32_e32 v2, v2, v5
.Lskip_compB:
	s_mov_b64 exec, -1
	v_add_u32_e32 v4, 64, v10
	v_lshlrev_b32_e32 v3, 1, v4
	v_lshl_or_b32 v3, v1, 10, v3
.LrestA_loop:
	v_cmp_gt_i32_e32 vcc, s27, v4
	s_and_b64 exec, exec, vcc
	s_cbranch_execz .LrestA_done
	ds_read_u16 v5, v3
	s_waitcnt lgkmcnt(0)
	v_add_u32_e32 v8, v6, v5
	v_lshlrev_b32_e32 v8, 4, v8
	global_load_dwordx4 v[12:15], v8, s[16:17] nt
	global_load_dwordx4 v[16:19], v8, s[18:19] nt
	v_lshlrev_b32_e32 v5, 4, v5
	ds_read_b128 v[20:23], v5 offset:32768
	s_waitcnt lgkmcnt(0)
	v_pk_add_f32 v[8:9], v[22:23], v[20:21] neg_lo:[0,1] neg_hi:[0,1]
	s_nop 0
	v_pk_fma_f32 v[20:21], v[8:9], 0.5, v[20:21] op_sel_hi:[1,0,1]
	s_waitcnt vmcnt(1)
	v_mul_f32_e32 v5, 0x3fb8aa3b, v14
	v_mul_f32_e32 v7, 0x3fb8aa3b, v15
	v_pk_fma_f32 v[12:13], v[12:13], v[8:9], v[20:21]
	s_waitcnt vmcnt(0)
	v_sub_f32_e32 v14, v18, v16
	v_sub_f32_e32 v20, v19, v17
	v_max_f32_e32 v11, v18, v18
	v_max_f32_e32 v15, v16, v16
	v_max_f32_e32 v18, v19, v19
	v_max_f32_e32 v19, v17, v17
	v_exp_f32_e32 v16, v5
	v_exp_f32_e32 v17, v7
	s_nop 0
	v_pk_mul_f32 v[8:9], v[16:17], v[8:9]
	s_nop 0
	v_pk_fma_f32 v[16:17], v[8:9], 0.5, v[12:13] op_sel_hi:[1,0,1] neg_lo:[1,0,0] neg_hi:[1,0,0]
	v_pk_fma_f32 v[8:9], v[8:9], 0.5, v[12:13] op_sel_hi:[1,0,1]
	v_max_f32_e32 v7, v16, v15
	v_min_f32_e32 v5, v8, v11
	v_min_f32_e32 v21, v9, v18
	v_max_f32_e32 v22, v17, v19
	v_pk_add_f32 v[12:13], v[8:9], v[16:17] neg_lo:[0,1] neg_hi:[0,1]
	v_max_f32_e32 v8, v8, v11
	v_min_f32_e32 v11, v16, v15
	v_max_f32_e32 v9, v9, v18
	v_min_f32_e32 v15, v17, v19
	v_sub_f32_e32 v5, v5, v7
	v_sub_f32_e32 v7, v21, v22
	v_sub_f32_e32 v8, v8, v11
	v_sub_f32_e32 v9, v9, v15
	v_max_f32_e32 v15, 0, v5
	v_max_f32_e32 v21, 0, v7
	v_max_f32_e32 v5, 0, v8
	v_max_f32_e32 v7, 0, v9
	v_pk_mul_f32 v[8:9], v[14:15], v[20:21]
	v_mul_f32_e32 v11, v5, v7
	v_fma_f32 v8, v12, v13, v8
	v_sub_f32_e32 v8, v8, v9
	v_rcp_f32_e32 v14, v11
	v_rcp_f32_e32 v15, v8
	v_fma_f32 v8, v5, v7, -v8
	v_pk_mul_f32 v[8:9], v[14:15], v[8:9]
	s_nop 0
	v_sub_f32_e32 v5, v8, v9
	v_add_f32_e32 v5, 1.0, v5
	v_add_f32_e32 v2, v2, v5
	v_add_u32_e32 v4, 64, v4
	v_add_u32_e32 v3, 0x80, v3
	s_branch .LrestA_loop
.LrestA_done:
	s_mov_b64 exec, -1
	v_add_u32_e32 v25, 64, v10
	v_lshlrev_b32_e32 v24, 1, v25
	v_lshl_or_b32 v24, v1, 10, v24
.LrestB_loop:
	v_cmp_gt_i32_e32 vcc, s28, v25
	s_and_b64 exec, exec, vcc
	s_cbranch_execz .LrestB_done
	ds_read_u16 v5, v24 offset:16384
	s_waitcnt lgkmcnt(0)
	v_add_u32_e32 v8, v43, v5
	v_lshlrev_b32_e32 v8, 4, v8
	global_load_dwordx4 v[12:15], v8, s[16:17] nt
	global_load_dwordx4 v[16:19], v8, s[18:19] nt
	v_lshlrev_b32_e32 v5, 4, v5
	ds_read_b128 v[20:23], v5 offset:40960
	s_waitcnt lgkmcnt(0)
	v_pk_add_f32 v[8:9], v[22:23], v[20:21] neg_lo:[0,1] neg_hi:[0,1]
	s_nop 0
	v_pk_fma_f32 v[20:21], v[8:9], 0.5, v[20:21] op_sel_hi:[1,0,1]
	s_waitcnt vmcnt(1)
	v_mul_f32_e32 v5, 0x3fb8aa3b, v14
	v_mul_f32_e32 v7, 0x3fb8aa3b, v15
	v_pk_fma_f32 v[12:13], v[12:13], v[8:9], v[20:21]
	s_waitcnt vmcnt(0)
	v_sub_f32_e32 v14, v18, v16
	v_sub_f32_e32 v20, v19, v17
	v_max_f32_e32 v11, v18, v18
	v_max_f32_e32 v15, v16, v16
	v_max_f32_e32 v18, v19, v19
	v_max_f32_e32 v19, v17, v17
	v_exp_f32_e32 v16, v5
	v_exp_f32_e32 v17, v7
	s_nop 0
	v_pk_mul_f32 v[8:9], v[16:17], v[8:9]
	s_nop 0
	v_pk_fma_f32 v[16:17], v[8:9], 0.5, v[12:13] op_sel_hi:[1,0,1] neg_lo:[1,0,0] neg_hi:[1,0,0]
	v_pk_fma_f32 v[8:9], v[8:9], 0.5, v[12:13] op_sel_hi:[1,0,1]
	v_max_f32_e32 v7, v16, v15
	v_min_f32_e32 v5, v8, v11
	v_min_f32_e32 v21, v9, v18
	v_max_f32_e32 v22, v17, v19
	v_pk_add_f32 v[12:13], v[8:9], v[16:17] neg_lo:[0,1] neg_hi:[0,1]
	v_max_f32_e32 v8, v8, v11
	v_min_f32_e32 v11, v16, v15
	v_max_f32_e32 v9, v9, v18
	v_min_f32_e32 v15, v17, v19
	v_sub_f32_e32 v5, v5, v7
	v_sub_f32_e32 v7, v21, v22
	v_sub_f32_e32 v8, v8, v11
	v_sub_f32_e32 v9, v9, v15
	v_max_f32_e32 v15, 0, v5
	v_max_f32_e32 v21, 0, v7
	v_max_f32_e32 v5, 0, v8
	v_max_f32_e32 v7, 0, v9
	v_pk_mul_f32 v[8:9], v[14:15], v[20:21]
	v_mul_f32_e32 v11, v5, v7
	v_fma_f32 v8, v12, v13, v8
	v_sub_f32_e32 v8, v8, v9
	v_rcp_f32_e32 v14, v11
	v_rcp_f32_e32 v15, v8
	v_fma_f32 v8, v5, v7, -v8
	v_pk_mul_f32 v[8:9], v[14:15], v[8:9]
	s_nop 0
	v_sub_f32_e32 v5, v8, v9
	v_add_f32_e32 v5, 1.0, v5
	v_add_f32_e32 v2, v2, v5
	v_add_u32_e32 v25, 64, v25
	v_add_u32_e32 v24, 0x80, v24
	s_branch .LrestB_loop
.LrestB_done:
.Lgather_done:
	s_mov_b64 exec, -1
	v_add_f32_dpp v2, v2, v2 quad_perm:[1,0,3,2] row_mask:0xf bank_mask:0xf bound_ctrl:1
	s_nop 1
	v_add_f32_dpp v2, v2, v2 quad_perm:[2,3,0,1] row_mask:0xf bank_mask:0xf bound_ctrl:1
	s_nop 1
	v_add_f32_dpp v2, v2, v2 row_half_mirror row_mask:0xf bank_mask:0xf bound_ctrl:1
	s_nop 1
	v_add_f32_dpp v2, v2, v2 row_mirror row_mask:0xf bank_mask:0xf bound_ctrl:1
	s_nop 1
	v_add_f32_dpp v2, v2, v2 row_bcast:15 row_mask:0xa bank_mask:0xf
	s_nop 1
	v_add_f32_dpp v2, v2, v2 row_bcast:31 row_mask:0xc bank_mask:0xf
	s_nop 0
	v_readlane_b32 s4, v2, 63
	s_add_i32 s3, s27, s28
	v_cvt_f32_i32_e32 v3, s3
	v_lshlrev_b32_e32 v4, 3, v1
	s_mov_b64 exec, 1
	v_mov_b32_e32 v2, s4
	ds_write_b64 v4, v[2:3] offset:49152
	s_mov_b64 exec, -1
	s_waitcnt lgkmcnt(0)
	s_barrier
	s_cmp_lg_u32 s15, 0
	s_cbranch_scc1 .Lpartial_end
	v_and_b32_e32 v4, 15, v10
	v_lshlrev_b32_e32 v4, 3, v4
	ds_read_b64 v[2:3], v4 offset:49152
	s_lshl_b32 s0, s2, 3
	v_mov_b32_e32 v5, s0
	s_waitcnt lgkmcnt(0)
	v_add_f32_dpp v2, v2, v2 quad_perm:[1,0,3,2] row_mask:0xf bank_mask:0xf bound_ctrl:1
	v_add_f32_dpp v3, v3, v3 quad_perm:[1,0,3,2] row_mask:0xf bank_mask:0xf bound_ctrl:1
	s_nop 0
	v_add_f32_dpp v2, v2, v2 quad_perm:[2,3,0,1] row_mask:0xf bank_mask:0xf bound_ctrl:1
	v_add_f32_dpp v3, v3, v3 quad_perm:[2,3,0,1] row_mask:0xf bank_mask:0xf bound_ctrl:1
	s_nop 0
	v_add_f32_dpp v2, v2, v2 row_half_mirror row_mask:0xf bank_mask:0xf bound_ctrl:1
	v_add_f32_dpp v3, v3, v3 row_half_mirror row_mask:0xf bank_mask:0xf bound_ctrl:1
	s_nop 0
	v_add_f32_dpp v2, v2, v2 row_mirror row_mask:0xf bank_mask:0xf bound_ctrl:1
	v_add_f32_dpp v3, v3, v3 row_mirror row_mask:0xf bank_mask:0xf bound_ctrl:1
	s_mov_b64 exec, 1
	global_store_dwordx2 v5, v[2:3], s[24:25]

.Llate_block:
	v_cmp_eq_u32_e32 vcc, 0, v0
	s_and_saveexec_b64 s[4:5], vcc
	s_cbranch_execz .Llate_end
	s_lshl_b32 s6, s2, 3
	v_mov_b32_e32 v2, 0
	v_mov_b32_e32 v3, 0
	v_mov_b32_e32 v4, s6
	s_waitcnt lgkmcnt(0)
	global_store_dwordx2 v4, v[2:3], s[24:25]

	.amdhsa_kernel _Z12giou_partialPK15HIP_vector_typeIfLj4EES2_S2_PKiPS_IfLj2EE
		.amdhsa_group_segment_fixed_size 49280
		.amdhsa_private_segment_fixed_size 0
		.amdhsa_kernarg_size 40
		.amdhsa_user_sgpr_count 2
		.amdhsa_user_sgpr_dispatch_ptr 0
		.amdhsa_user_sgpr_queue_ptr 0
		.amdhsa_user_sgpr_kernarg_segment_ptr 1
		.amdhsa_user_sgpr_dispatch_id 0
		.amdhsa_user_sgpr_kernarg_preload_length 0
		.amdhsa_user_sgpr_kernarg_preload_offset 0
		.amdhsa_user_sgpr_private_segment_size 0
		.amdhsa_uses_dynamic_stack 0
		.amdhsa_enable_private_segment 0
		.amdhsa_system_sgpr_workgroup_id_x 1
		.amdhsa_system_sgpr_workgroup_id_y 0
		.amdhsa_system_sgpr_workgroup_id_z 0
		.amdhsa_system_sgpr_workgroup_info 0
		.amdhsa_system_vgpr_workitem_id 0
		.amdhsa_next_free_vgpr 48
		.amdhsa_next_free_sgpr 34
		.amdhsa_accum_offset 48
		.amdhsa_reserve_vcc 1
		.amdhsa_float_round_mode_32 0
		.amdhsa_float_round_mode_16_64 0
		.amdhsa_float_denorm_mode_32 3
		.amdhsa_float_denorm_mode_16_64 3
		.amdhsa_dx10_clamp 1
		.amdhsa_ieee_mode 1
		.amdhsa_fp16_overflow 0
		.amdhsa_tg_split 0
		.amdhsa_exception_fp_ieee_invalid_op 0
		.amdhsa_exception_fp_denorm_src 0
		.amdhsa_exception_fp_ieee_div_zero 0
		.amdhsa_exception_fp_ieee_overflow 0
		.amdhsa_exception_fp_ieee_underflow 0
		.amdhsa_exception_fp_ieee_inexact 0
		.amdhsa_exception_int_div_zero 0
	.end_amdhsa_kernel

.Lfunc_end0:
	.size	_Z12giou_partialPK15HIP_vector_typeIfLj4EES2_S2_PKiPS_IfLj2EE, .Lfunc_end0-_Z12giou_partialPK15HIP_vector_typeIfLj4EES2_S2_PKiPS_IfLj2EE
	.set _Z12giou_partialPK15HIP_vector_typeIfLj4EES2_S2_PKiPS_IfLj2EE.num_vgpr, 48
	.set _Z12giou_partialPK15HIP_vector_typeIfLj4EES2_S2_PKiPS_IfLj2EE.num_agpr, 0
	.set _Z12giou_partialPK15HIP_vector_typeIfLj4EES2_S2_PKiPS_IfLj2EE.numbered_sgpr, 34
	.set _Z12giou_partialPK15HIP_vector_typeIfLj4EES2_S2_PKiPS_IfLj2EE.num_named_barrier, 0
	.set _Z12giou_partialPK15HIP_vector_typeIfLj4EES2_S2_PKiPS_IfLj2EE.private_seg_size, 0
	.set _Z12giou_partialPK15HIP_vector_typeIfLj4EES2_S2_PKiPS_IfLj2EE.uses_vcc, 1
	.set _Z12giou_partialPK15HIP_vector_typeIfLj4EES2_S2_PKiPS_IfLj2EE.uses_flat_scratch, 0
	.set _Z12giou_partialPK15HIP_vector_typeIfLj4EES2_S2_PKiPS_IfLj2EE.has_dyn_sized_stack, 0
	.set _Z12giou_partialPK15HIP_vector_typeIfLj4EES2_S2_PKiPS_IfLj2EE.has_recursion, 0
	.set _Z12giou_partialPK15HIP_vector_typeIfLj4EES2_S2_PKiPS_IfLj2EE.has_indirect_call, 0

amdhsa.kernels:
  - .agpr_count:     0
    .args:
      - .actual_access:  read_only
        .address_space:  global
        .offset:         0
        .size:           8
        .value_kind:     global_buffer
      - .actual_access:  read_only
        .address_space:  global
        .offset:         8
        .size:           8
        .value_kind:     global_buffer
      - .actual_access:  read_only
        .address_space:  global
        .offset:         16
        .size:           8
        .value_kind:     global_buffer
      - .actual_access:  read_only
        .address_space:  global
        .offset:         24
        .size:           8
        .value_kind:     global_buffer
      - .actual_access:  write_only
        .address_space:  global
        .offset:         32
        .size:           8
        .value_kind:     global_buffer
    .group_segment_fixed_size: 49280
    .kernarg_segment_align: 8
    .kernarg_segment_size: 40
    .language:       OpenCL C
    .language_version:
      - 2
      - 0
    .max_flat_workgroup_size: 1024
    .name:           _Z12giou_partialPK15HIP_vector_typeIfLj4EES2_S2_PKiPS_IfLj2EE
    .private_segment_fixed_size: 0
    .sgpr_count:     40
    .sgpr_spill_count: 0
    .symbol:         _Z12giou_partialPK15HIP_vector_typeIfLj4EES2_S2_PKiPS_IfLj2EE.kd
    .uniform_work_group_size: 1
    .uses_dynamic_stack: false
    .vgpr_count:     48
    .vgpr_spill_count: 0
    .wavefront_size: 64
  - .agpr_count:     0
    .args:
      - .actual_access:  read_only
        .address_space:  global
        .offset:         0
        .size:           8
        .value_kind:     global_buffer
      - .actual_access:  write_only
        .address_space:  global
        .offset:         8
        .size:           8
        .value_kind:     global_buffer
    .group_segment_fixed_size: 0
    .kernarg_segment_align: 8
    .kernarg_segment_size: 16
    .language:       OpenCL C
    .language_version:
      - 2
      - 0
    .max_flat_workgroup_size: 64
    .name:           _Z10giou_finalPK15HIP_vector_typeIfLj2EEPf
    .private_segment_fixed_size: 0
    .sgpr_count:     18
    .sgpr_spill_count: 0
    .symbol:         _Z10giou_finalPK15HIP_vector_typeIfLj2EEPf.kd
    .uniform_work_group_size: 1
    .uses_dynamic_stack: false
    .vgpr_count:     18
    .vgpr_spill_count: 0
    .wavefront_size: 64
